# grid barrier: non-leader workgroups poll the cross-XCD release word directly (one hop less)
# baseline (speedup 1.0000x reference)
; __device__ __forceinline__ unsigned xb_ld(unsigned* p)              { return __hip_atomic_load(p, __ATOMIC_RELAXED, __HIP_MEMORY_SCOPE_AGENT); }
; __device__ __forceinline__ unsigned xb_add(unsigned* p, unsigned v) { return __hip_atomic_fetch_add(p, v, __ATOMIC_RELAXED, __HIP_MEMORY_SCOPE_AGENT); }
; #define XB_SPIN(cond, bar) do { unsigned _sp = 0; while (cond) { __builtin_amdgcn_s_sleep(1); \
;     if ((++_sp & 255u) == 0u) { if (xb_ld(&(bar)[XB_TMO])) break; if (_sp > XB_SPIN_CAP) { atomicAdd(&(bar)[XB_TMO], 1u); break; } } } } while (0)
; __device__ __forceinline__ void xcd_barrier(const XcdBarrier& b) {
;     ...
;         const unsigned old = xb_add(&bar[XB_XSUB(b.x)], 1u);
;         const unsigned gen = old / nloc;
;         if (old + 1u == (gen + 1u) * nloc) {
;             __builtin_amdgcn_fence(__ATOMIC_RELEASE, "agent");
;             asm volatile("s_waitcnt vmcnt(0)" ::: "memory");
;             const unsigned og = xb_add(&bar[XB_TOP], 1u);
;             const unsigned tg = og / nx;
;             if (og + 1u == (tg + 1u) * nx) xb_add(&bar[XB_TOPGEN], 1u);
;             else XB_SPIN(xb_ld(&bar[XB_TOPGEN]) == tg, bar);
;             __builtin_amdgcn_fence(__ATOMIC_ACQUIRE, "agent");
;             xb_add(&bar[XB_XGEN(b.x)], 1u);
;             asm volatile("s_waitcnt vmcnt(0)" ::: "memory");
;         } else {
;             XB_SPIN(xb_ld(&bar[XB_XGEN(b.x)]) == gen, bar);
;             __builtin_amdgcn_fence(__ATOMIC_ACQUIRE, "agent");
.LBB0_220:
	s_or_b64 exec, exec, s[12:13]
	v_cvt_f32_u32_e32 v4, v2
	s_waitcnt vmcnt(0)
	v_readfirstlane_b32 s0, v3
	v_sub_u32_e32 v3, 0, v2
	v_rcp_iflag_f32_e32 v4, v4
	v_add_u32_e32 v5, s0, v1
	v_mul_f32_e32 v4, 0x4f7ffffe, v4
	v_cvt_u32_f32_e32 v4, v4
	v_mul_lo_u32 v1, v3, v4
	v_mul_hi_u32 v1, v4, v1
	v_add_u32_e32 v1, v4, v1
	v_mul_hi_u32 v1, v5, v1
	v_mul_lo_u32 v3, v1, v2
	v_sub_u32_e32 v3, v5, v3
	v_add_u32_e32 v4, 1, v1
	v_sub_u32_e32 v6, v3, v2
	v_cmp_ge_u32_e32 vcc, v3, v2
	s_nop 1
	v_cndmask_b32_e32 v1, v1, v4, vcc
	v_cndmask_b32_e32 v3, v3, v6, vcc
	v_add_u32_e32 v4, 1, v1
	v_cmp_ge_u32_e32 vcc, v3, v2
	v_add_u32_e32 v3, 1, v5
	s_nop 0
	v_cndmask_b32_e32 v1, v1, v4, vcc
	v_mul_lo_u32 v4, v2, v1
	v_add_u32_e32 v2, v4, v2
	v_cmp_ne_u32_e32 vcc, v3, v2
	s_and_saveexec_b64 s[0:1], vcc
	s_xor_b64 s[10:11], exec, s[0:1]
	s_cbranch_execz .LBB0_234
	s_waitcnt lgkmcnt(0)
	v_readlane_b32 s98, v254, 53
	v_mov_b32_e32 v0, 0
	s_lshl_b32 s98, s98, 8
	s_sub_u32 s98, s8, s98
	s_subb_u32 s99, s9, 0
	s_add_u32 s16, s98, 0x3500
	s_addc_u32 s17, s99, 0
	global_load_dword v0, v0, s[16:17] sc1
	s_waitcnt vmcnt(0)
	v_cmp_eq_u32_e32 vcc, v0, v1
	s_and_saveexec_b64 s[12:13], vcc
	s_cbranch_execz .LBB0_233
	s_mov_b32 s0, 1
	s_mov_b64 s[20:21], 0
	v_mov_b32_e32 v0, 0
	s_branch .LBB0_224

; __device__ __forceinline__ unsigned xb_ld(unsigned* p)              { return __hip_atomic_load(p, __ATOMIC_RELAXED, __HIP_MEMORY_SCOPE_AGENT); }
; __device__ __forceinline__ unsigned xb_add(unsigned* p, unsigned v) { return __hip_atomic_fetch_add(p, v, __ATOMIC_RELAXED, __HIP_MEMORY_SCOPE_AGENT); }
; #define XB_SPIN(cond, bar) do { unsigned _sp = 0; while (cond) { __builtin_amdgcn_s_sleep(1); \
;     if ((++_sp & 255u) == 0u) { if (xb_ld(&(bar)[XB_TMO])) break; if (_sp > XB_SPIN_CAP) { atomicAdd(&(bar)[XB_TMO], 1u); break; } } } } while (0)
; __device__ __forceinline__ void xcd_barrier(const XcdBarrier& b) {
;     ...
;         const unsigned old = xb_add(&bar[XB_XSUB(b.x)], 1u);
;         const unsigned gen = old / nloc;
;         if (old + 1u == (gen + 1u) * nloc) {
;             __builtin_amdgcn_fence(__ATOMIC_RELEASE, "agent");
;             asm volatile("s_waitcnt vmcnt(0)" ::: "memory");
;             const unsigned og = xb_add(&bar[XB_TOP], 1u);
;             const unsigned tg = og / nx;
;             if (og + 1u == (tg + 1u) * nx) xb_add(&bar[XB_TOPGEN], 1u);
;             else XB_SPIN(xb_ld(&bar[XB_TOPGEN]) == tg, bar);
;             __builtin_amdgcn_fence(__ATOMIC_ACQUIRE, "agent");
;             xb_add(&bar[XB_XGEN(b.x)], 1u);
;             asm volatile("s_waitcnt vmcnt(0)" ::: "memory");
;         } else {
;             XB_SPIN(xb_ld(&bar[XB_XGEN(b.x)]) == gen, bar);
;             __builtin_amdgcn_fence(__ATOMIC_ACQUIRE, "agent");
.LBB0_718:
	s_or_b64 exec, exec, s[8:9]
	v_cvt_f32_u32_e32 v4, v2
	s_waitcnt vmcnt(0)
	v_readfirstlane_b32 s4, v3
	v_sub_u32_e32 v3, 0, v2
	v_rcp_iflag_f32_e32 v4, v4
	v_add_u32_e32 v5, s4, v0
	v_mul_f32_e32 v4, 0x4f7ffffe, v4
	v_cvt_u32_f32_e32 v4, v4
	v_mul_lo_u32 v0, v3, v4
	v_mul_hi_u32 v0, v4, v0
	v_add_u32_e32 v0, v4, v0
	v_mul_hi_u32 v0, v5, v0
	v_mul_lo_u32 v3, v0, v2
	v_sub_u32_e32 v3, v5, v3
	v_add_u32_e32 v4, 1, v0
	v_cmp_ge_u32_e32 vcc, v3, v2
	s_nop 1
	v_cndmask_b32_e32 v0, v0, v4, vcc
	v_sub_u32_e32 v4, v3, v2
	v_cndmask_b32_e32 v3, v3, v4, vcc
	v_add_u32_e32 v4, 1, v0
	v_cmp_ge_u32_e32 vcc, v3, v2
	v_add_u32_e32 v3, 1, v5
	s_nop 0
	v_cndmask_b32_e32 v0, v0, v4, vcc
	v_mul_lo_u32 v4, v2, v0
	v_add_u32_e32 v2, v4, v2
	v_cmp_ne_u32_e32 vcc, v3, v2
	s_and_saveexec_b64 s[4:5], vcc
	s_xor_b64 s[4:5], exec, s[4:5]
	s_cbranch_execz .LBB0_732
	s_waitcnt lgkmcnt(0)
	v_readlane_b32 s98, v255, 16
	v_mov_b32_e32 v1, 0
	s_lshl_b32 s98, s98, 8
	s_sub_u32 s98, s2, s98
	s_subb_u32 s99, s3, 0
	s_add_u32 s12, s98, 0x3500
	s_addc_u32 s13, s99, 0
	global_load_dword v1, v1, s[12:13] sc1
	s_waitcnt vmcnt(0)
	v_cmp_eq_u32_e32 vcc, v1, v0
	s_and_saveexec_b64 s[8:9], vcc
	s_cbranch_execz .LBB0_731
	v_readlane_b32 s20, v254, 35
	v_readlane_b32 s21, v254, 36
	s_add_u32 s10, s20, 0x3800
	s_addc_u32 s11, s21, 0
	s_mov_b32 s28, 1
	s_mov_b64 s[16:17], 0
	v_mov_b32_e32 v1, 0
	v_readlane_b32 s22, v254, 37
	v_readlane_b32 s23, v254, 38
	s_branch .LBB0_722

; __device__ __forceinline__ unsigned xb_ld(unsigned* p)              { return __hip_atomic_load(p, __ATOMIC_RELAXED, __HIP_MEMORY_SCOPE_AGENT); }
; __device__ __forceinline__ unsigned xb_add(unsigned* p, unsigned v) { return __hip_atomic_fetch_add(p, v, __ATOMIC_RELAXED, __HIP_MEMORY_SCOPE_AGENT); }
; #define XB_SPIN(cond, bar) do { unsigned _sp = 0; while (cond) { __builtin_amdgcn_s_sleep(1); \
;     if ((++_sp & 255u) == 0u) { if (xb_ld(&(bar)[XB_TMO])) break; if (_sp > XB_SPIN_CAP) { atomicAdd(&(bar)[XB_TMO], 1u); break; } } } } while (0)
; __device__ __forceinline__ void xcd_barrier(const XcdBarrier& b) {
;     ...
;         const unsigned old = xb_add(&bar[XB_XSUB(b.x)], 1u);
;         const unsigned gen = old / nloc;
;         if (old + 1u == (gen + 1u) * nloc) {
;             __builtin_amdgcn_fence(__ATOMIC_RELEASE, "agent");
;             asm volatile("s_waitcnt vmcnt(0)" ::: "memory");
;             const unsigned og = xb_add(&bar[XB_TOP], 1u);
;             const unsigned tg = og / nx;
;             if (og + 1u == (tg + 1u) * nx) xb_add(&bar[XB_TOPGEN], 1u);
;             else XB_SPIN(xb_ld(&bar[XB_TOPGEN]) == tg, bar);
;             __builtin_amdgcn_fence(__ATOMIC_ACQUIRE, "agent");
;             xb_add(&bar[XB_XGEN(b.x)], 1u);
;             asm volatile("s_waitcnt vmcnt(0)" ::: "memory");
;         } else {
;             XB_SPIN(xb_ld(&bar[XB_XGEN(b.x)]) == gen, bar);
;             __builtin_amdgcn_fence(__ATOMIC_ACQUIRE, "agent");
.LBB0_773:
	s_or_b64 exec, exec, s[8:9]
	v_cvt_f32_u32_e32 v4, v2
	s_waitcnt vmcnt(0)
	v_readfirstlane_b32 s4, v3
	v_sub_u32_e32 v3, 0, v2
	v_rcp_iflag_f32_e32 v4, v4
	v_add_u32_e32 v5, s4, v0
	v_mul_f32_e32 v4, 0x4f7ffffe, v4
	v_cvt_u32_f32_e32 v4, v4
	v_mul_lo_u32 v0, v3, v4
	v_mul_hi_u32 v0, v4, v0
	v_add_u32_e32 v0, v4, v0
	v_mul_hi_u32 v0, v5, v0
	v_mul_lo_u32 v3, v0, v2
	v_sub_u32_e32 v3, v5, v3
	v_add_u32_e32 v4, 1, v0
	v_cmp_ge_u32_e32 vcc, v3, v2
	s_nop 1
	v_cndmask_b32_e32 v0, v0, v4, vcc
	v_sub_u32_e32 v4, v3, v2
	v_cndmask_b32_e32 v3, v3, v4, vcc
	v_add_u32_e32 v4, 1, v0
	v_cmp_ge_u32_e32 vcc, v3, v2
	v_add_u32_e32 v3, 1, v5
	s_nop 0
	v_cndmask_b32_e32 v0, v0, v4, vcc
	v_mul_lo_u32 v4, v2, v0
	v_add_u32_e32 v2, v4, v2
	v_cmp_ne_u32_e32 vcc, v3, v2
	s_and_saveexec_b64 s[4:5], vcc
	s_xor_b64 s[4:5], exec, s[4:5]
	s_cbranch_execz .LBB0_787
	s_waitcnt lgkmcnt(0)
	v_readlane_b32 s98, v255, 16
	v_mov_b32_e32 v1, 0
	s_lshl_b32 s98, s98, 8
	s_sub_u32 s98, s2, s98
	s_subb_u32 s99, s3, 0
	s_add_u32 s12, s98, 0x3500
	s_addc_u32 s13, s99, 0
	global_load_dword v1, v1, s[12:13] sc1
	s_waitcnt vmcnt(0)
	v_cmp_eq_u32_e32 vcc, v1, v0
	s_and_saveexec_b64 s[8:9], vcc
	s_cbranch_execz .LBB0_786
	v_readlane_b32 s16, v254, 35
	v_readlane_b32 s17, v254, 36
	s_add_u32 s10, s16, 0x3800
	s_addc_u32 s11, s17, 0
	s_mov_b32 s24, 1
	s_mov_b64 s[14:15], 0
	v_mov_b32_e32 v1, 0
	v_readlane_b32 s18, v254, 37
	v_readlane_b32 s19, v254, 38
	s_branch .LBB0_777

; __device__ __forceinline__ unsigned xb_ld(unsigned* p)              { return __hip_atomic_load(p, __ATOMIC_RELAXED, __HIP_MEMORY_SCOPE_AGENT); }
; __device__ __forceinline__ unsigned xb_add(unsigned* p, unsigned v) { return __hip_atomic_fetch_add(p, v, __ATOMIC_RELAXED, __HIP_MEMORY_SCOPE_AGENT); }
; #define XB_SPIN(cond, bar) do { unsigned _sp = 0; while (cond) { __builtin_amdgcn_s_sleep(1); \
;     if ((++_sp & 255u) == 0u) { if (xb_ld(&(bar)[XB_TMO])) break; if (_sp > XB_SPIN_CAP) { atomicAdd(&(bar)[XB_TMO], 1u); break; } } } } while (0)
; __device__ __forceinline__ void xcd_barrier(const XcdBarrier& b) {
;     ...
;         const unsigned old = xb_add(&bar[XB_XSUB(b.x)], 1u);
;         const unsigned gen = old / nloc;
;         if (old + 1u == (gen + 1u) * nloc) {
;             __builtin_amdgcn_fence(__ATOMIC_RELEASE, "agent");
;             asm volatile("s_waitcnt vmcnt(0)" ::: "memory");
;             const unsigned og = xb_add(&bar[XB_TOP], 1u);
;             const unsigned tg = og / nx;
;             if (og + 1u == (tg + 1u) * nx) xb_add(&bar[XB_TOPGEN], 1u);
;             else XB_SPIN(xb_ld(&bar[XB_TOPGEN]) == tg, bar);
;             __builtin_amdgcn_fence(__ATOMIC_ACQUIRE, "agent");
;             xb_add(&bar[XB_XGEN(b.x)], 1u);
;             asm volatile("s_waitcnt vmcnt(0)" ::: "memory");
;         } else {
;             XB_SPIN(xb_ld(&bar[XB_XGEN(b.x)]) == gen, bar);
;             __builtin_amdgcn_fence(__ATOMIC_ACQUIRE, "agent");
.LBB0_977:
	s_or_b64 exec, exec, s[6:7]
	v_cvt_f32_u32_e32 v4, v2
	s_waitcnt vmcnt(0)
	v_readfirstlane_b32 s4, v3
	v_sub_u32_e32 v3, 0, v2
	v_rcp_iflag_f32_e32 v4, v4
	v_add_u32_e32 v5, s4, v0
	v_mul_f32_e32 v4, 0x4f7ffffe, v4
	v_cvt_u32_f32_e32 v4, v4
	v_mul_lo_u32 v0, v3, v4
	v_mul_hi_u32 v0, v4, v0
	v_add_u32_e32 v0, v4, v0
	v_mul_hi_u32 v0, v5, v0
	v_mul_lo_u32 v3, v0, v2
	v_sub_u32_e32 v3, v5, v3
	v_add_u32_e32 v4, 1, v0
	v_cmp_ge_u32_e32 vcc, v3, v2
	s_nop 1
	v_cndmask_b32_e32 v0, v0, v4, vcc
	v_sub_u32_e32 v4, v3, v2
	v_cndmask_b32_e32 v3, v3, v4, vcc
	v_add_u32_e32 v4, 1, v0
	v_cmp_ge_u32_e32 vcc, v3, v2
	v_add_u32_e32 v3, 1, v5
	s_nop 0
	v_cndmask_b32_e32 v0, v0, v4, vcc
	v_mul_lo_u32 v4, v2, v0
	v_add_u32_e32 v2, v4, v2
	v_cmp_ne_u32_e32 vcc, v3, v2
	s_and_saveexec_b64 s[4:5], vcc
	s_xor_b64 s[4:5], exec, s[4:5]
	s_cbranch_execz .LBB0_991
	s_waitcnt lgkmcnt(0)
	v_readlane_b32 s98, v255, 16
	v_mov_b32_e32 v1, 0
	s_lshl_b32 s98, s98, 8
	s_sub_u32 s98, s2, s98
	s_subb_u32 s99, s3, 0
	s_add_u32 s10, s98, 0x3500
	s_addc_u32 s11, s99, 0
	global_load_dword v1, v1, s[10:11] sc1
	s_waitcnt vmcnt(0)
	v_cmp_eq_u32_e32 vcc, v1, v0
	s_and_saveexec_b64 s[6:7], vcc
	s_cbranch_execz .LBB0_990
	v_readlane_b32 s12, v254, 35
	v_readlane_b32 s13, v254, 36
	s_add_u32 s8, s12, 0x3800
	v_readlane_b32 s14, v254, 37
	v_readlane_b32 s15, v254, 38
	s_addc_u32 s9, s13, 0
	s_mov_b32 s22, 1
	s_mov_b64 s[12:13], 0
	v_mov_b32_e32 v1, 0
	s_branch .LBB0_981

; __device__ __forceinline__ unsigned xb_ld(unsigned* p)              { return __hip_atomic_load(p, __ATOMIC_RELAXED, __HIP_MEMORY_SCOPE_AGENT); }
; __device__ __forceinline__ unsigned xb_add(unsigned* p, unsigned v) { return __hip_atomic_fetch_add(p, v, __ATOMIC_RELAXED, __HIP_MEMORY_SCOPE_AGENT); }
; #define XB_SPIN(cond, bar) do { unsigned _sp = 0; while (cond) { __builtin_amdgcn_s_sleep(1); \
;     if ((++_sp & 255u) == 0u) { if (xb_ld(&(bar)[XB_TMO])) break; if (_sp > XB_SPIN_CAP) { atomicAdd(&(bar)[XB_TMO], 1u); break; } } } } while (0)
; __device__ __forceinline__ void xcd_barrier(const XcdBarrier& b) {
;     ...
;         const unsigned old = xb_add(&bar[XB_XSUB(b.x)], 1u);
;         const unsigned gen = old / nloc;
;         if (old + 1u == (gen + 1u) * nloc) {
;             __builtin_amdgcn_fence(__ATOMIC_RELEASE, "agent");
;             asm volatile("s_waitcnt vmcnt(0)" ::: "memory");
;             const unsigned og = xb_add(&bar[XB_TOP], 1u);
;             const unsigned tg = og / nx;
;             if (og + 1u == (tg + 1u) * nx) xb_add(&bar[XB_TOPGEN], 1u);
;             else XB_SPIN(xb_ld(&bar[XB_TOPGEN]) == tg, bar);
;             __builtin_amdgcn_fence(__ATOMIC_ACQUIRE, "agent");
;             xb_add(&bar[XB_XGEN(b.x)], 1u);
;             asm volatile("s_waitcnt vmcnt(0)" ::: "memory");
;         } else {
;             XB_SPIN(xb_ld(&bar[XB_XGEN(b.x)]) == gen, bar);
;             __builtin_amdgcn_fence(__ATOMIC_ACQUIRE, "agent");
.LBB0_1225:
	s_or_b64 exec, exec, s[6:7]
	v_cvt_f32_u32_e32 v4, v2
	s_waitcnt vmcnt(0)
	v_readfirstlane_b32 s4, v3
	v_sub_u32_e32 v3, 0, v2
	v_rcp_iflag_f32_e32 v4, v4
	v_add_u32_e32 v5, s4, v1
	v_mul_f32_e32 v4, 0x4f7ffffe, v4
	v_cvt_u32_f32_e32 v4, v4
	v_mul_lo_u32 v1, v3, v4
	v_mul_hi_u32 v1, v4, v1
	v_add_u32_e32 v1, v4, v1
	v_mul_hi_u32 v1, v5, v1
	v_mul_lo_u32 v3, v1, v2
	v_sub_u32_e32 v3, v5, v3
	v_add_u32_e32 v4, 1, v1
	v_cmp_ge_u32_e32 vcc, v3, v2
	s_nop 1
	v_cndmask_b32_e32 v1, v1, v4, vcc
	v_sub_u32_e32 v4, v3, v2
	v_cndmask_b32_e32 v3, v3, v4, vcc
	v_add_u32_e32 v4, 1, v1
	v_cmp_ge_u32_e32 vcc, v3, v2
	v_add_u32_e32 v3, 1, v5
	s_nop 0
	v_cndmask_b32_e32 v1, v1, v4, vcc
	v_mul_lo_u32 v4, v2, v1
	v_add_u32_e32 v2, v4, v2
	v_cmp_ne_u32_e32 vcc, v3, v2
	s_and_saveexec_b64 s[4:5], vcc
	s_xor_b64 s[4:5], exec, s[4:5]
	s_cbranch_execz .LBB0_1240
	s_waitcnt lgkmcnt(0)
	v_readlane_b32 s98, v254, 53
	v_mov_b32_e32 v0, 0
	s_lshl_b32 s98, s98, 8
	s_sub_u32 s98, s2, s98
	s_subb_u32 s99, s3, 0
	s_add_u32 s8, s98, 0x3500
	s_addc_u32 s9, s99, 0
	global_load_dword v0, v0, s[8:9] sc1
	s_waitcnt vmcnt(0)
	v_cmp_eq_u32_e32 vcc, v0, v1
	s_and_saveexec_b64 s[6:7], vcc
	s_cbranch_execz .LBB0_1239
	s_mov_b32 s20, 1
	s_mov_b64 s[10:11], 0
	v_mov_b32_e32 v0, 0
	s_branch .LBB0_1229
